# P6 U sweep: the eight h rows of a token group stay resident in registers (no per-token-change reloads); 8-way unpack switch
# speedup vs baseline: 1.0221x; 1.0088x over previous
.Lp6_b8_done:
	s_mov_b64 exec, s[14:15]
	s_waitcnt vmcnt(0)
	v_mov_b32_e32 v1, s85
	ds_read_b32 v1, v1 offset:4864
	s_mov_b32 s0, s33
	s_ashr_i32 s1, s33, 31
	s_lshl_b64 s[0:1], s[0:1], 11
	s_waitcnt lgkmcnt(0)
	v_readfirstlane_b32 s26, v1
	v_lshl_add_u64 v[142:143], v[76:77], 0, s[0:1]
	s_movk_i32 s88, 0
	v_lshl_add_u64 v[12:13], v[142:143], 0, s[88:89]
	global_load_dwordx4 v[78:81], v[12:13], off offset:0
	global_load_dwordx4 v[82:85], v[12:13], off offset:16
	global_load_dwordx4 v[86:89], v[12:13], off offset:2048
	global_load_dwordx4 v[90:93], v[12:13], off offset:2064
	s_movk_i32 s88, 4096
	v_lshl_add_u64 v[12:13], v[142:143], 0, s[88:89]
	global_load_dwordx4 v[94:97], v[12:13], off offset:0
	global_load_dwordx4 v[98:101], v[12:13], off offset:16
	global_load_dwordx4 v[102:105], v[12:13], off offset:2048
	global_load_dwordx4 v[106:109], v[12:13], off offset:2064
	s_movk_i32 s88, 8192
	v_lshl_add_u64 v[12:13], v[142:143], 0, s[88:89]
	global_load_dwordx4 v[110:113], v[12:13], off offset:0
	global_load_dwordx4 v[114:117], v[12:13], off offset:16
	global_load_dwordx4 v[118:121], v[12:13], off offset:2048
	global_load_dwordx4 v[122:125], v[12:13], off offset:2064
	s_movk_i32 s88, 12288
	v_lshl_add_u64 v[12:13], v[142:143], 0, s[88:89]
	global_load_dwordx4 v[126:129], v[12:13], off offset:0
	global_load_dwordx4 v[130:133], v[12:13], off offset:16
	global_load_dwordx4 v[134:137], v[12:13], off offset:2048
	global_load_dwordx4 v[138:141], v[12:13], off offset:2064
	s_mov_b32 s88, 0
	s_and_b32 s2, s26, 0x3ff
	s_bfe_u32 s3, s26, 0x4000a
	v_cmp_gt_u32_e32 vcc, s3, v182
	s_lshl_b32 s2, s2, 2
	s_add_i32 s2, s2, s85
	v_cndmask_b32_e32 v1, 0, v182, vcc
	v_lshl_add_u32 v1, v1, 2, s2
	ds_read_b32 v1, v1 offset:8192
	s_waitcnt lgkmcnt(0)
	v_lshlrev_b32_e32 v1, 10, v1
	v_and_b32_e32 v1, 0x3fffc00, v1
	s_nop 0
	v_readlane_b32 s44, v1, 0
	v_readlane_b32 s45, v1, 1
	v_readlane_b32 s46, v1, 2
	v_readlane_b32 s47, v1, 3
	v_readlane_b32 s48, v1, 4
	v_readlane_b32 s49, v1, 5
	v_readlane_b32 s50, v1, 6
	v_readlane_b32 s51, v1, 7
	s_nop 4
	buffer_load_dwordx4 v[68:71], v181, s[8:11], s44 offen
	buffer_load_dwordx4 v[64:67], v181, s[8:11], s45 offen
	buffer_load_dwordx4 v[60:63], v181, s[8:11], s46 offen
	buffer_load_dwordx4 v[56:59], v181, s[8:11], s47 offen
	buffer_load_dwordx4 v[48:51], v181, s[8:11], s48 offen
	buffer_load_dwordx4 v[32:35], v181, s[8:11], s49 offen
	buffer_load_dwordx4 v[16:19], v181, s[8:11], s50 offen
	buffer_load_dwordx4 v[12:15], v181, s[8:11], s51 offen
	s_add_i32 s3, s22, -1
	s_min_i32 s2, s3, 1
	s_max_i32 s2, s2, 0
	s_lshl_b32 s2, s2, 2
	s_add_i32 s2, s85, s2
	v_mov_b32_e32 v1, s2
	ds_read_b32 v1, v1 offset:4864
	s_waitcnt lgkmcnt(0)
	v_readfirstlane_b32 s86, v1
	s_and_b32 s2, s86, 0x3ff
	s_bfe_u32 s3, s86, 0x4000a
	v_cmp_gt_u32_e32 vcc, s3, v182
	s_lshl_b32 s2, s2, 2
	s_add_i32 s2, s2, s85
	v_cndmask_b32_e32 v1, 0, v182, vcc
	v_lshl_add_u32 v1, v1, 2, s2
	ds_read_b32 v1, v1 offset:8192
	s_waitcnt lgkmcnt(0)
	v_lshlrev_b32_e32 v1, 10, v1
	v_and_b32_e32 v1, 0x3fffc00, v1
	s_nop 0
	v_readlane_b32 s44, v1, 0
	v_readlane_b32 s45, v1, 1
	v_readlane_b32 s46, v1, 2
	v_readlane_b32 s47, v1, 3
	v_readlane_b32 s48, v1, 4
	v_readlane_b32 s49, v1, 5
	v_readlane_b32 s50, v1, 6
	v_readlane_b32 s51, v1, 7
	s_nop 4
	buffer_load_dwordx4 v[72:75], v181, s[8:11], s44 offen
	buffer_load_dwordx4 v[52:55], v181, s[8:11], s45 offen
	buffer_load_dwordx4 v[44:47], v181, s[8:11], s46 offen
	buffer_load_dwordx4 v[40:43], v181, s[8:11], s47 offen
	buffer_load_dwordx4 v[36:39], v181, s[8:11], s48 offen
	buffer_load_dwordx4 v[28:31], v181, s[8:11], s49 offen
	buffer_load_dwordx4 v[24:27], v181, s[8:11], s50 offen
	buffer_load_dwordx4 v[20:23], v181, s[8:11], s51 offen
	s_add_i32 s3, s22, -1
	s_min_i32 s2, s3, 2
	s_max_i32 s2, s2, 0
	s_lshl_b32 s2, s2, 2
	s_add_i32 s2, s85, s2
	v_mov_b32_e32 v1, s2
	ds_read_b32 v1, v1 offset:4864
	s_waitcnt lgkmcnt(0)
	v_readfirstlane_b32 s27, v1
	s_and_b32 s2, s27, 0x3ff
	s_bfe_u32 s3, s27, 0x4000a
	v_cmp_gt_u32_e32 vcc, s3, v182
	s_lshl_b32 s2, s2, 2
	s_add_i32 s2, s2, s85
	v_cndmask_b32_e32 v1, 0, v182, vcc
	v_lshl_add_u32 v1, v1, 2, s2
	ds_read_b32 v1, v1 offset:8192
	s_waitcnt lgkmcnt(0)
	v_lshlrev_b32_e32 v1, 10, v1
	v_and_b32_e32 v1, 0x3fffc00, v1
	s_nop 0
	v_readlane_b32 s44, v1, 0
	v_readlane_b32 s45, v1, 1
	v_readlane_b32 s46, v1, 2
	v_readlane_b32 s47, v1, 3
	v_readlane_b32 s48, v1, 4
	v_readlane_b32 s49, v1, 5
	v_readlane_b32 s50, v1, 6
	v_readlane_b32 s51, v1, 7
	s_nop 4
	buffer_load_dwordx4 v[224:227], v181, s[8:11], s44 offen
	buffer_load_dwordx4 v[228:231], v181, s[8:11], s45 offen
	buffer_load_dwordx4 v[232:235], v181, s[8:11], s46 offen
	buffer_load_dwordx4 v[236:239], v181, s[8:11], s47 offen
	buffer_load_dwordx4 v[240:243], v181, s[8:11], s48 offen
	buffer_load_dwordx4 v[244:247], v181, s[8:11], s49 offen
	buffer_load_dwordx4 v[248:251], v181, s[8:11], s50 offen
	buffer_load_dwordx4 v[216:219], v181, s[8:11], s51 offen
	s_add_i32 s3, s22, -1
	s_min_i32 s2, s3, 3
	s_max_i32 s2, s2, 0
	s_lshl_b32 s2, s2, 2
	s_add_i32 s2, s85, s2
	v_mov_b32_e32 v1, s2
	ds_read_b32 v1, v1 offset:4864
	s_waitcnt lgkmcnt(0)
	v_readfirstlane_b32 s32, v1
	s_mov_b32 s23, 0
	s_mov_b64 s[0:1], -1
.Lp6a0_top:
	s_add_i32 s23, s23, 1
	s_add_i32 s2, s23, 3
	s_add_i32 s3, s22, -1
	s_min_i32 s2, s2, s3
	s_lshl_b32 s2, s2, 2
	s_add_i32 s2, s85, s2
	v_mov_b32_e32 v1, s2
	ds_read_b32 v252, v1 offset:4864
	s_and_b32 s2, s32, 0x3ff
	s_bfe_u32 s3, s32, 0x4000a
	v_cmp_gt_u32_e32 vcc, s3, v182
	s_lshl_b32 s2, s2, 2
	s_add_i32 s2, s2, s85
	v_cndmask_b32_e32 v1, 0, v182, vcc
	v_lshl_add_u32 v1, v1, 2, s2
	ds_read_b32 v1, v1 offset:8192
	s_and_b32 s2, s26, 0x3ff
	v_add_u32_e32 v210, s2, v180
	v_lshl_add_u32 v210, v210, 2, s85
	ds_read_b32 v196, v210
	s_waitcnt vmcnt(16)
	s_andn2_b64 vcc, exec, s[0:1]
	s_waitcnt lgkmcnt(0)
	v_readfirstlane_b32 s37, v252
	v_lshlrev_b32_e32 v1, 10, v1
	v_and_b32_e32 v1, 0x3fffc00, v1
	s_nop 0
	v_readlane_b32 s44, v1, 0
	v_readlane_b32 s45, v1, 1
	v_readlane_b32 s46, v1, 2
	v_readlane_b32 s47, v1, 3
	v_readlane_b32 s48, v1, 4
	v_readlane_b32 s49, v1, 5
	v_readlane_b32 s50, v1, 6
	v_readlane_b32 s51, v1, 7
	s_cbranch_vccnz .Lp6a0_954
	s_lshr_b32 s66, s26, 14
	s_cmp_eq_u32 s66, 0
	s_cbranch_scc1 .Lp6a0_u0
	s_cmp_eq_u32 s66, 1
	s_cbranch_scc1 .Lp6a0_u1
	s_cmp_eq_u32 s66, 2
	s_cbranch_scc1 .Lp6a0_u2
	s_cmp_eq_u32 s66, 3
	s_cbranch_scc1 .Lp6a0_u3
	s_cmp_eq_u32 s66, 4
	s_cbranch_scc1 .Lp6a0_u4
	s_cmp_eq_u32 s66, 5
	s_cbranch_scc1 .Lp6a0_u5
	s_cmp_eq_u32 s66, 6
	s_cbranch_scc1 .Lp6a0_u6
	s_branch .Lp6a0_u7
.Lp6a0_u0:
	v_lshlrev_b32_e32 v144, 16, v78
	v_and_b32_e32 v145, 0xffff0000, v78
	v_lshlrev_b32_e32 v146, 16, v79
	v_and_b32_e32 v147, 0xffff0000, v79
	v_lshlrev_b32_e32 v148, 16, v80
	v_and_b32_e32 v149, 0xffff0000, v80
	v_lshlrev_b32_e32 v150, 16, v81
	v_and_b32_e32 v151, 0xffff0000, v81
	v_lshlrev_b32_e32 v152, 16, v82
	v_and_b32_e32 v153, 0xffff0000, v82
	v_lshlrev_b32_e32 v154, 16, v83
	v_and_b32_e32 v155, 0xffff0000, v83
	v_lshlrev_b32_e32 v156, 16, v84
	v_and_b32_e32 v157, 0xffff0000, v84
	v_lshlrev_b32_e32 v158, 16, v85
	v_and_b32_e32 v159, 0xffff0000, v85
	s_branch .Lp6a0_954
.Lp6a0_u1:
	v_lshlrev_b32_e32 v144, 16, v86
	v_and_b32_e32 v145, 0xffff0000, v86
	v_lshlrev_b32_e32 v146, 16, v87
	v_and_b32_e32 v147, 0xffff0000, v87
	v_lshlrev_b32_e32 v148, 16, v88
	v_and_b32_e32 v149, 0xffff0000, v88
	v_lshlrev_b32_e32 v150, 16, v89
	v_and_b32_e32 v151, 0xffff0000, v89
	v_lshlrev_b32_e32 v152, 16, v90
	v_and_b32_e32 v153, 0xffff0000, v90
	v_lshlrev_b32_e32 v154, 16, v91
	v_and_b32_e32 v155, 0xffff0000, v91
	v_lshlrev_b32_e32 v156, 16, v92
	v_and_b32_e32 v157, 0xffff0000, v92
	v_lshlrev_b32_e32 v158, 16, v93
	v_and_b32_e32 v159, 0xffff0000, v93
	s_branch .Lp6a0_954
.Lp6a0_u2:
	v_lshlrev_b32_e32 v144, 16, v94
	v_and_b32_e32 v145, 0xffff0000, v94
	v_lshlrev_b32_e32 v146, 16, v95
	v_and_b32_e32 v147, 0xffff0000, v95
	v_lshlrev_b32_e32 v148, 16, v96
	v_and_b32_e32 v149, 0xffff0000, v96
	v_lshlrev_b32_e32 v150, 16, v97
	v_and_b32_e32 v151, 0xffff0000, v97
	v_lshlrev_b32_e32 v152, 16, v98
	v_and_b32_e32 v153, 0xffff0000, v98
	v_lshlrev_b32_e32 v154, 16, v99
	v_and_b32_e32 v155, 0xffff0000, v99
	v_lshlrev_b32_e32 v156, 16, v100
	v_and_b32_e32 v157, 0xffff0000, v100
	v_lshlrev_b32_e32 v158, 16, v101
	v_and_b32_e32 v159, 0xffff0000, v101
	s_branch .Lp6a0_954
.Lp6a0_u3:
	v_lshlrev_b32_e32 v144, 16, v102
	v_and_b32_e32 v145, 0xffff0000, v102
	v_lshlrev_b32_e32 v146, 16, v103
	v_and_b32_e32 v147, 0xffff0000, v103
	v_lshlrev_b32_e32 v148, 16, v104
	v_and_b32_e32 v149, 0xffff0000, v104
	v_lshlrev_b32_e32 v150, 16, v105
	v_and_b32_e32 v151, 0xffff0000, v105
	v_lshlrev_b32_e32 v152, 16, v106
	v_and_b32_e32 v153, 0xffff0000, v106
	v_lshlrev_b32_e32 v154, 16, v107
	v_and_b32_e32 v155, 0xffff0000, v107
	v_lshlrev_b32_e32 v156, 16, v108
	v_and_b32_e32 v157, 0xffff0000, v108
	v_lshlrev_b32_e32 v158, 16, v109
	v_and_b32_e32 v159, 0xffff0000, v109
	s_branch .Lp6a0_954
.Lp6a0_u4:
	v_lshlrev_b32_e32 v144, 16, v110
	v_and_b32_e32 v145, 0xffff0000, v110
	v_lshlrev_b32_e32 v146, 16, v111
	v_and_b32_e32 v147, 0xffff0000, v111
	v_lshlrev_b32_e32 v148, 16, v112
	v_and_b32_e32 v149, 0xffff0000, v112
	v_lshlrev_b32_e32 v150, 16, v113
	v_and_b32_e32 v151, 0xffff0000, v113
	v_lshlrev_b32_e32 v152, 16, v114
	v_and_b32_e32 v153, 0xffff0000, v114
	v_lshlrev_b32_e32 v154, 16, v115
	v_and_b32_e32 v155, 0xffff0000, v115
	v_lshlrev_b32_e32 v156, 16, v116
	v_and_b32_e32 v157, 0xffff0000, v116
	v_lshlrev_b32_e32 v158, 16, v117
	v_and_b32_e32 v159, 0xffff0000, v117
	s_branch .Lp6a0_954
.Lp6a0_u5:
	v_lshlrev_b32_e32 v144, 16, v118
	v_and_b32_e32 v145, 0xffff0000, v118
	v_lshlrev_b32_e32 v146, 16, v119
	v_and_b32_e32 v147, 0xffff0000, v119
	v_lshlrev_b32_e32 v148, 16, v120
	v_and_b32_e32 v149, 0xffff0000, v120
	v_lshlrev_b32_e32 v150, 16, v121
	v_and_b32_e32 v151, 0xffff0000, v121
	v_lshlrev_b32_e32 v152, 16, v122
	v_and_b32_e32 v153, 0xffff0000, v122
	v_lshlrev_b32_e32 v154, 16, v123
	v_and_b32_e32 v155, 0xffff0000, v123
	v_lshlrev_b32_e32 v156, 16, v124
	v_and_b32_e32 v157, 0xffff0000, v124
	v_lshlrev_b32_e32 v158, 16, v125
	v_and_b32_e32 v159, 0xffff0000, v125
	s_branch .Lp6a0_954
.Lp6a0_u6:
	v_lshlrev_b32_e32 v144, 16, v126
	v_and_b32_e32 v145, 0xffff0000, v126
	v_lshlrev_b32_e32 v146, 16, v127
	v_and_b32_e32 v147, 0xffff0000, v127
	v_lshlrev_b32_e32 v148, 16, v128
	v_and_b32_e32 v149, 0xffff0000, v128
	v_lshlrev_b32_e32 v150, 16, v129
	v_and_b32_e32 v151, 0xffff0000, v129
	v_lshlrev_b32_e32 v152, 16, v130
	v_and_b32_e32 v153, 0xffff0000, v130
	v_lshlrev_b32_e32 v154, 16, v131
	v_and_b32_e32 v155, 0xffff0000, v131
	v_lshlrev_b32_e32 v156, 16, v132
	v_and_b32_e32 v157, 0xffff0000, v132
	v_lshlrev_b32_e32 v158, 16, v133
	v_and_b32_e32 v159, 0xffff0000, v133
	s_branch .Lp6a0_954
.Lp6a0_u7:
	v_lshlrev_b32_e32 v144, 16, v134
	v_and_b32_e32 v145, 0xffff0000, v134
	v_lshlrev_b32_e32 v146, 16, v135
	v_and_b32_e32 v147, 0xffff0000, v135
	v_lshlrev_b32_e32 v148, 16, v136
	v_and_b32_e32 v149, 0xffff0000, v136
	v_lshlrev_b32_e32 v150, 16, v137
	v_and_b32_e32 v151, 0xffff0000, v137
	v_lshlrev_b32_e32 v152, 16, v138
	v_and_b32_e32 v153, 0xffff0000, v138
	v_lshlrev_b32_e32 v154, 16, v139
	v_and_b32_e32 v155, 0xffff0000, v139
	v_lshlrev_b32_e32 v156, 16, v140
	v_and_b32_e32 v157, 0xffff0000, v140
	v_lshlrev_b32_e32 v158, 16, v141
	v_and_b32_e32 v159, 0xffff0000, v141
.Lp6a0_954:
	s_lshr_b32 s66, s26, 14
	s_lshr_b32 s14, s86, 14
	s_cmp_lg_u32 s14, s66
	s_cselect_b64 s[0:1], -1, 0
.Lp6a0_956:
	s_bfe_u32 s36, s26, 0x4000a
	v_cvt_pk_f32_fp8_e32 v[184:185], v68
	v_cvt_pk_f32_fp8_e32 v[192:193], v64
	v_cvt_pk_f32_fp8_sdwa v[186:187], v68 src0_sel:WORD_1
	v_cvt_pk_f32_fp8_sdwa v[194:195], v64 src0_sel:WORD_1
	v_pk_mul_f32 v[188:189], v[184:185], v[144:145]
	v_pk_mul_f32 v[222:223], v[192:193], v[144:145]
	v_pk_mul_f32 v[190:191], v[186:187], v[146:147]
	v_pk_mul_f32 v[176:177], v[194:195], v[146:147]
	v_cvt_pk_f32_fp8_e32 v[184:185], v69
	v_cvt_pk_f32_fp8_e32 v[192:193], v65
	v_cvt_pk_f32_fp8_sdwa v[186:187], v69 src0_sel:WORD_1
	v_cvt_pk_f32_fp8_sdwa v[194:195], v65 src0_sel:WORD_1
	v_pk_fma_f32 v[188:189], v[184:185], v[148:149], v[188:189]
	v_pk_fma_f32 v[222:223], v[192:193], v[148:149], v[222:223]
	v_pk_fma_f32 v[190:191], v[186:187], v[150:151], v[190:191]
	v_pk_fma_f32 v[176:177], v[194:195], v[150:151], v[176:177]
	v_cvt_pk_f32_fp8_e32 v[184:185], v70
	v_cvt_pk_f32_fp8_e32 v[192:193], v66
	v_cvt_pk_f32_fp8_sdwa v[186:187], v70 src0_sel:WORD_1
	v_cvt_pk_f32_fp8_sdwa v[194:195], v66 src0_sel:WORD_1
	v_pk_fma_f32 v[188:189], v[184:185], v[152:153], v[188:189]
	v_pk_fma_f32 v[222:223], v[192:193], v[152:153], v[222:223]
	v_pk_fma_f32 v[190:191], v[186:187], v[154:155], v[190:191]
	v_pk_fma_f32 v[176:177], v[194:195], v[154:155], v[176:177]
	v_cvt_pk_f32_fp8_e32 v[184:185], v71
	v_cvt_pk_f32_fp8_e32 v[192:193], v67
	v_cvt_pk_f32_fp8_sdwa v[186:187], v71 src0_sel:WORD_1
	v_cvt_pk_f32_fp8_sdwa v[194:195], v67 src0_sel:WORD_1
	v_pk_fma_f32 v[188:189], v[184:185], v[156:157], v[188:189]
	v_pk_fma_f32 v[222:223], v[192:193], v[156:157], v[222:223]
	v_pk_fma_f32 v[190:191], v[186:187], v[158:159], v[190:191]
	v_pk_fma_f32 v[176:177], v[194:195], v[158:159], v[176:177]
	v_pk_add_f32 v[188:189], v[188:189], v[190:191]
	v_pk_add_f32 v[222:223], v[222:223], v[176:177]
	v_add_f32_e32 v160, v188, v189
	v_add_f32_e32 v162, v222, v223
	s_cmp_le_u32 s36, 2
	s_cbranch_scc1 .Lp6a0_dotdone
	v_cvt_pk_f32_fp8_e32 v[184:185], v60
	v_cvt_pk_f32_fp8_e32 v[192:193], v56
	v_cvt_pk_f32_fp8_sdwa v[186:187], v60 src0_sel:WORD_1
	v_cvt_pk_f32_fp8_sdwa v[194:195], v56 src0_sel:WORD_1
	v_pk_mul_f32 v[188:189], v[184:185], v[144:145]
	v_pk_mul_f32 v[222:223], v[192:193], v[144:145]
	v_pk_mul_f32 v[190:191], v[186:187], v[146:147]
	v_pk_mul_f32 v[176:177], v[194:195], v[146:147]
	v_cvt_pk_f32_fp8_e32 v[184:185], v61
	v_cvt_pk_f32_fp8_e32 v[192:193], v57
	v_cvt_pk_f32_fp8_sdwa v[186:187], v61 src0_sel:WORD_1
	v_cvt_pk_f32_fp8_sdwa v[194:195], v57 src0_sel:WORD_1
	v_pk_fma_f32 v[188:189], v[184:185], v[148:149], v[188:189]
	v_pk_fma_f32 v[222:223], v[192:193], v[148:149], v[222:223]
	v_pk_fma_f32 v[190:191], v[186:187], v[150:151], v[190:191]
	v_pk_fma_f32 v[176:177], v[194:195], v[150:151], v[176:177]
	v_cvt_pk_f32_fp8_e32 v[184:185], v62
	v_cvt_pk_f32_fp8_e32 v[192:193], v58
	v_cvt_pk_f32_fp8_sdwa v[186:187], v62 src0_sel:WORD_1
	v_cvt_pk_f32_fp8_sdwa v[194:195], v58 src0_sel:WORD_1
	v_pk_fma_f32 v[188:189], v[184:185], v[152:153], v[188:189]
	v_pk_fma_f32 v[222:223], v[192:193], v[152:153], v[222:223]
	v_pk_fma_f32 v[190:191], v[186:187], v[154:155], v[190:191]
	v_pk_fma_f32 v[176:177], v[194:195], v[154:155], v[176:177]
	v_cvt_pk_f32_fp8_e32 v[184:185], v63
	v_cvt_pk_f32_fp8_e32 v[192:193], v59
	v_cvt_pk_f32_fp8_sdwa v[186:187], v63 src0_sel:WORD_1
	v_cvt_pk_f32_fp8_sdwa v[194:195], v59 src0_sel:WORD_1
	v_pk_fma_f32 v[188:189], v[184:185], v[156:157], v[188:189]
	v_pk_fma_f32 v[222:223], v[192:193], v[156:157], v[222:223]
	v_pk_fma_f32 v[190:191], v[186:187], v[158:159], v[190:191]
	v_pk_fma_f32 v[176:177], v[194:195], v[158:159], v[176:177]
	v_pk_add_f32 v[188:189], v[188:189], v[190:191]
	v_pk_add_f32 v[222:223], v[222:223], v[176:177]
	v_add_f32_e32 v164, v188, v189
	v_add_f32_e32 v166, v222, v223
	s_cmp_le_u32 s36, 4
	s_cbranch_scc1 .Lp6a0_dotdone
	v_cvt_pk_f32_fp8_e32 v[184:185], v48
	v_cvt_pk_f32_fp8_e32 v[192:193], v32
	v_cvt_pk_f32_fp8_sdwa v[186:187], v48 src0_sel:WORD_1
	v_cvt_pk_f32_fp8_sdwa v[194:195], v32 src0_sel:WORD_1
	v_pk_mul_f32 v[188:189], v[184:185], v[144:145]
	v_pk_mul_f32 v[222:223], v[192:193], v[144:145]
	v_pk_mul_f32 v[190:191], v[186:187], v[146:147]
	v_pk_mul_f32 v[176:177], v[194:195], v[146:147]
	v_cvt_pk_f32_fp8_e32 v[184:185], v49
	v_cvt_pk_f32_fp8_e32 v[192:193], v33
	v_cvt_pk_f32_fp8_sdwa v[186:187], v49 src0_sel:WORD_1
	v_cvt_pk_f32_fp8_sdwa v[194:195], v33 src0_sel:WORD_1
	v_pk_fma_f32 v[188:189], v[184:185], v[148:149], v[188:189]
	v_pk_fma_f32 v[222:223], v[192:193], v[148:149], v[222:223]
	v_pk_fma_f32 v[190:191], v[186:187], v[150:151], v[190:191]
	v_pk_fma_f32 v[176:177], v[194:195], v[150:151], v[176:177]
	v_cvt_pk_f32_fp8_e32 v[184:185], v50
	v_cvt_pk_f32_fp8_e32 v[192:193], v34
	v_cvt_pk_f32_fp8_sdwa v[186:187], v50 src0_sel:WORD_1
	v_cvt_pk_f32_fp8_sdwa v[194:195], v34 src0_sel:WORD_1
	v_pk_fma_f32 v[188:189], v[184:185], v[152:153], v[188:189]
	v_pk_fma_f32 v[222:223], v[192:193], v[152:153], v[222:223]
	v_pk_fma_f32 v[190:191], v[186:187], v[154:155], v[190:191]
	v_pk_fma_f32 v[176:177], v[194:195], v[154:155], v[176:177]
	v_cvt_pk_f32_fp8_e32 v[184:185], v51
	v_cvt_pk_f32_fp8_e32 v[192:193], v35
	v_cvt_pk_f32_fp8_sdwa v[186:187], v51 src0_sel:WORD_1
	v_cvt_pk_f32_fp8_sdwa v[194:195], v35 src0_sel:WORD_1
	v_pk_fma_f32 v[188:189], v[184:185], v[156:157], v[188:189]
	v_pk_fma_f32 v[222:223], v[192:193], v[156:157], v[222:223]
	v_pk_fma_f32 v[190:191], v[186:187], v[158:159], v[190:191]
	v_pk_fma_f32 v[176:177], v[194:195], v[158:159], v[176:177]
	v_pk_add_f32 v[188:189], v[188:189], v[190:191]
	v_pk_add_f32 v[222:223], v[222:223], v[176:177]
	v_add_f32_e32 v168, v188, v189
	v_add_f32_e32 v170, v222, v223
	s_cmp_le_u32 s36, 6
	s_cbranch_scc1 .Lp6a0_dotdone
	v_cvt_pk_f32_fp8_e32 v[184:185], v16
	v_cvt_pk_f32_fp8_e32 v[192:193], v12
	v_cvt_pk_f32_fp8_sdwa v[186:187], v16 src0_sel:WORD_1
	v_cvt_pk_f32_fp8_sdwa v[194:195], v12 src0_sel:WORD_1
	v_pk_mul_f32 v[188:189], v[184:185], v[144:145]
	v_pk_mul_f32 v[222:223], v[192:193], v[144:145]
	v_pk_mul_f32 v[190:191], v[186:187], v[146:147]
	v_pk_mul_f32 v[176:177], v[194:195], v[146:147]
	v_cvt_pk_f32_fp8_e32 v[184:185], v17
	v_cvt_pk_f32_fp8_e32 v[192:193], v13
	v_cvt_pk_f32_fp8_sdwa v[186:187], v17 src0_sel:WORD_1
	v_cvt_pk_f32_fp8_sdwa v[194:195], v13 src0_sel:WORD_1
	v_pk_fma_f32 v[188:189], v[184:185], v[148:149], v[188:189]
	v_pk_fma_f32 v[222:223], v[192:193], v[148:149], v[222:223]
	v_pk_fma_f32 v[190:191], v[186:187], v[150:151], v[190:191]
	v_pk_fma_f32 v[176:177], v[194:195], v[150:151], v[176:177]
	v_cvt_pk_f32_fp8_e32 v[184:185], v18
	v_cvt_pk_f32_fp8_e32 v[192:193], v14
	v_cvt_pk_f32_fp8_sdwa v[186:187], v18 src0_sel:WORD_1
	v_cvt_pk_f32_fp8_sdwa v[194:195], v14 src0_sel:WORD_1
	v_pk_fma_f32 v[188:189], v[184:185], v[152:153], v[188:189]
	v_pk_fma_f32 v[222:223], v[192:193], v[152:153], v[222:223]
	v_pk_fma_f32 v[190:191], v[186:187], v[154:155], v[190:191]
	v_pk_fma_f32 v[176:177], v[194:195], v[154:155], v[176:177]
	v_cvt_pk_f32_fp8_e32 v[184:185], v19
	v_cvt_pk_f32_fp8_e32 v[192:193], v15
	v_cvt_pk_f32_fp8_sdwa v[186:187], v19 src0_sel:WORD_1
	v_cvt_pk_f32_fp8_sdwa v[194:195], v15 src0_sel:WORD_1
	v_pk_fma_f32 v[188:189], v[184:185], v[156:157], v[188:189]
	v_pk_fma_f32 v[222:223], v[192:193], v[156:157], v[222:223]
	v_pk_fma_f32 v[190:191], v[186:187], v[158:159], v[190:191]
	v_pk_fma_f32 v[176:177], v[194:195], v[158:159], v[176:177]
	v_pk_add_f32 v[188:189], v[188:189], v[190:191]
	v_pk_add_f32 v[222:223], v[222:223], v[176:177]
	v_add_f32_e32 v172, v188, v189
	v_add_f32_e32 v174, v222, v223

.Lp6a1_954:
	s_lshr_b32 s66, s26, 14
	s_lshr_b32 s14, s86, 14
	s_cmp_lg_u32 s14, s66
	s_cselect_b64 s[0:1], -1, 0
.Lp6a1_956:
	s_bfe_u32 s36, s26, 0x4000a
	v_cvt_pk_f32_fp8_e32 v[184:185], v72
	v_cvt_pk_f32_fp8_e32 v[192:193], v52
	v_cvt_pk_f32_fp8_sdwa v[186:187], v72 src0_sel:WORD_1
	v_cvt_pk_f32_fp8_sdwa v[194:195], v52 src0_sel:WORD_1
	v_pk_mul_f32 v[188:189], v[184:185], v[144:145]
	v_pk_mul_f32 v[222:223], v[192:193], v[144:145]
	v_pk_mul_f32 v[190:191], v[186:187], v[146:147]
	v_pk_mul_f32 v[176:177], v[194:195], v[146:147]
	v_cvt_pk_f32_fp8_e32 v[184:185], v73
	v_cvt_pk_f32_fp8_e32 v[192:193], v53
	v_cvt_pk_f32_fp8_sdwa v[186:187], v73 src0_sel:WORD_1
	v_cvt_pk_f32_fp8_sdwa v[194:195], v53 src0_sel:WORD_1
	v_pk_fma_f32 v[188:189], v[184:185], v[148:149], v[188:189]
	v_pk_fma_f32 v[222:223], v[192:193], v[148:149], v[222:223]
	v_pk_fma_f32 v[190:191], v[186:187], v[150:151], v[190:191]
	v_pk_fma_f32 v[176:177], v[194:195], v[150:151], v[176:177]
	v_cvt_pk_f32_fp8_e32 v[184:185], v74
	v_cvt_pk_f32_fp8_e32 v[192:193], v54
	v_cvt_pk_f32_fp8_sdwa v[186:187], v74 src0_sel:WORD_1
	v_cvt_pk_f32_fp8_sdwa v[194:195], v54 src0_sel:WORD_1
	v_pk_fma_f32 v[188:189], v[184:185], v[152:153], v[188:189]
	v_pk_fma_f32 v[222:223], v[192:193], v[152:153], v[222:223]
	v_pk_fma_f32 v[190:191], v[186:187], v[154:155], v[190:191]
	v_pk_fma_f32 v[176:177], v[194:195], v[154:155], v[176:177]
	v_cvt_pk_f32_fp8_e32 v[184:185], v75
	v_cvt_pk_f32_fp8_e32 v[192:193], v55
	v_cvt_pk_f32_fp8_sdwa v[186:187], v75 src0_sel:WORD_1
	v_cvt_pk_f32_fp8_sdwa v[194:195], v55 src0_sel:WORD_1
	v_pk_fma_f32 v[188:189], v[184:185], v[156:157], v[188:189]
	v_pk_fma_f32 v[222:223], v[192:193], v[156:157], v[222:223]
	v_pk_fma_f32 v[190:191], v[186:187], v[158:159], v[190:191]
	v_pk_fma_f32 v[176:177], v[194:195], v[158:159], v[176:177]
	v_pk_add_f32 v[188:189], v[188:189], v[190:191]
	v_pk_add_f32 v[222:223], v[222:223], v[176:177]
	v_add_f32_e32 v160, v188, v189
	v_add_f32_e32 v162, v222, v223
	s_cmp_le_u32 s36, 2
	s_cbranch_scc1 .Lp6a1_dotdone
	v_cvt_pk_f32_fp8_e32 v[184:185], v44
	v_cvt_pk_f32_fp8_e32 v[192:193], v40
	v_cvt_pk_f32_fp8_sdwa v[186:187], v44 src0_sel:WORD_1
	v_cvt_pk_f32_fp8_sdwa v[194:195], v40 src0_sel:WORD_1
	v_pk_mul_f32 v[188:189], v[184:185], v[144:145]
	v_pk_mul_f32 v[222:223], v[192:193], v[144:145]
	v_pk_mul_f32 v[190:191], v[186:187], v[146:147]
	v_pk_mul_f32 v[176:177], v[194:195], v[146:147]
	v_cvt_pk_f32_fp8_e32 v[184:185], v45
	v_cvt_pk_f32_fp8_e32 v[192:193], v41
	v_cvt_pk_f32_fp8_sdwa v[186:187], v45 src0_sel:WORD_1
	v_cvt_pk_f32_fp8_sdwa v[194:195], v41 src0_sel:WORD_1
	v_pk_fma_f32 v[188:189], v[184:185], v[148:149], v[188:189]
	v_pk_fma_f32 v[222:223], v[192:193], v[148:149], v[222:223]
	v_pk_fma_f32 v[190:191], v[186:187], v[150:151], v[190:191]
	v_pk_fma_f32 v[176:177], v[194:195], v[150:151], v[176:177]
	v_cvt_pk_f32_fp8_e32 v[184:185], v46
	v_cvt_pk_f32_fp8_e32 v[192:193], v42
	v_cvt_pk_f32_fp8_sdwa v[186:187], v46 src0_sel:WORD_1
	v_cvt_pk_f32_fp8_sdwa v[194:195], v42 src0_sel:WORD_1
	v_pk_fma_f32 v[188:189], v[184:185], v[152:153], v[188:189]
	v_pk_fma_f32 v[222:223], v[192:193], v[152:153], v[222:223]
	v_pk_fma_f32 v[190:191], v[186:187], v[154:155], v[190:191]
	v_pk_fma_f32 v[176:177], v[194:195], v[154:155], v[176:177]
	v_cvt_pk_f32_fp8_e32 v[184:185], v47
	v_cvt_pk_f32_fp8_e32 v[192:193], v43
	v_cvt_pk_f32_fp8_sdwa v[186:187], v47 src0_sel:WORD_1
	v_cvt_pk_f32_fp8_sdwa v[194:195], v43 src0_sel:WORD_1
	v_pk_fma_f32 v[188:189], v[184:185], v[156:157], v[188:189]
	v_pk_fma_f32 v[222:223], v[192:193], v[156:157], v[222:223]
	v_pk_fma_f32 v[190:191], v[186:187], v[158:159], v[190:191]
	v_pk_fma_f32 v[176:177], v[194:195], v[158:159], v[176:177]
	v_pk_add_f32 v[188:189], v[188:189], v[190:191]
	v_pk_add_f32 v[222:223], v[222:223], v[176:177]
	v_add_f32_e32 v164, v188, v189
	v_add_f32_e32 v166, v222, v223
	s_cmp_le_u32 s36, 4
	s_cbranch_scc1 .Lp6a1_dotdone
	v_cvt_pk_f32_fp8_e32 v[184:185], v36
	v_cvt_pk_f32_fp8_e32 v[192:193], v28
	v_cvt_pk_f32_fp8_sdwa v[186:187], v36 src0_sel:WORD_1
	v_cvt_pk_f32_fp8_sdwa v[194:195], v28 src0_sel:WORD_1
	v_pk_mul_f32 v[188:189], v[184:185], v[144:145]
	v_pk_mul_f32 v[222:223], v[192:193], v[144:145]
	v_pk_mul_f32 v[190:191], v[186:187], v[146:147]
	v_pk_mul_f32 v[176:177], v[194:195], v[146:147]
	v_cvt_pk_f32_fp8_e32 v[184:185], v37
	v_cvt_pk_f32_fp8_e32 v[192:193], v29
	v_cvt_pk_f32_fp8_sdwa v[186:187], v37 src0_sel:WORD_1
	v_cvt_pk_f32_fp8_sdwa v[194:195], v29 src0_sel:WORD_1
	v_pk_fma_f32 v[188:189], v[184:185], v[148:149], v[188:189]
	v_pk_fma_f32 v[222:223], v[192:193], v[148:149], v[222:223]
	v_pk_fma_f32 v[190:191], v[186:187], v[150:151], v[190:191]
	v_pk_fma_f32 v[176:177], v[194:195], v[150:151], v[176:177]
	v_cvt_pk_f32_fp8_e32 v[184:185], v38
	v_cvt_pk_f32_fp8_e32 v[192:193], v30
	v_cvt_pk_f32_fp8_sdwa v[186:187], v38 src0_sel:WORD_1
	v_cvt_pk_f32_fp8_sdwa v[194:195], v30 src0_sel:WORD_1
	v_pk_fma_f32 v[188:189], v[184:185], v[152:153], v[188:189]
	v_pk_fma_f32 v[222:223], v[192:193], v[152:153], v[222:223]
	v_pk_fma_f32 v[190:191], v[186:187], v[154:155], v[190:191]
	v_pk_fma_f32 v[176:177], v[194:195], v[154:155], v[176:177]
	v_cvt_pk_f32_fp8_e32 v[184:185], v39
	v_cvt_pk_f32_fp8_e32 v[192:193], v31
	v_cvt_pk_f32_fp8_sdwa v[186:187], v39 src0_sel:WORD_1
	v_cvt_pk_f32_fp8_sdwa v[194:195], v31 src0_sel:WORD_1
	v_pk_fma_f32 v[188:189], v[184:185], v[156:157], v[188:189]
	v_pk_fma_f32 v[222:223], v[192:193], v[156:157], v[222:223]
	v_pk_fma_f32 v[190:191], v[186:187], v[158:159], v[190:191]
	v_pk_fma_f32 v[176:177], v[194:195], v[158:159], v[176:177]
	v_pk_add_f32 v[188:189], v[188:189], v[190:191]
	v_pk_add_f32 v[222:223], v[222:223], v[176:177]
	v_add_f32_e32 v168, v188, v189
	v_add_f32_e32 v170, v222, v223
	s_cmp_le_u32 s36, 6
	s_cbranch_scc1 .Lp6a1_dotdone
	v_cvt_pk_f32_fp8_e32 v[184:185], v24
	v_cvt_pk_f32_fp8_e32 v[192:193], v20
	v_cvt_pk_f32_fp8_sdwa v[186:187], v24 src0_sel:WORD_1
	v_cvt_pk_f32_fp8_sdwa v[194:195], v20 src0_sel:WORD_1
	v_pk_mul_f32 v[188:189], v[184:185], v[144:145]
	v_pk_mul_f32 v[222:223], v[192:193], v[144:145]
	v_pk_mul_f32 v[190:191], v[186:187], v[146:147]
	v_pk_mul_f32 v[176:177], v[194:195], v[146:147]
	v_cvt_pk_f32_fp8_e32 v[184:185], v25
	v_cvt_pk_f32_fp8_e32 v[192:193], v21
	v_cvt_pk_f32_fp8_sdwa v[186:187], v25 src0_sel:WORD_1
	v_cvt_pk_f32_fp8_sdwa v[194:195], v21 src0_sel:WORD_1
	v_pk_fma_f32 v[188:189], v[184:185], v[148:149], v[188:189]
	v_pk_fma_f32 v[222:223], v[192:193], v[148:149], v[222:223]
	v_pk_fma_f32 v[190:191], v[186:187], v[150:151], v[190:191]
	v_pk_fma_f32 v[176:177], v[194:195], v[150:151], v[176:177]
	v_cvt_pk_f32_fp8_e32 v[184:185], v26
	v_cvt_pk_f32_fp8_e32 v[192:193], v22
	v_cvt_pk_f32_fp8_sdwa v[186:187], v26 src0_sel:WORD_1
	v_cvt_pk_f32_fp8_sdwa v[194:195], v22 src0_sel:WORD_1
	v_pk_fma_f32 v[188:189], v[184:185], v[152:153], v[188:189]
	v_pk_fma_f32 v[222:223], v[192:193], v[152:153], v[222:223]
	v_pk_fma_f32 v[190:191], v[186:187], v[154:155], v[190:191]
	v_pk_fma_f32 v[176:177], v[194:195], v[154:155], v[176:177]
	v_cvt_pk_f32_fp8_e32 v[184:185], v27
	v_cvt_pk_f32_fp8_e32 v[192:193], v23
	v_cvt_pk_f32_fp8_sdwa v[186:187], v27 src0_sel:WORD_1
	v_cvt_pk_f32_fp8_sdwa v[194:195], v23 src0_sel:WORD_1
	v_pk_fma_f32 v[188:189], v[184:185], v[156:157], v[188:189]
	v_pk_fma_f32 v[222:223], v[192:193], v[156:157], v[222:223]
	v_pk_fma_f32 v[190:191], v[186:187], v[158:159], v[190:191]
	v_pk_fma_f32 v[176:177], v[194:195], v[158:159], v[176:177]
	v_pk_add_f32 v[188:189], v[188:189], v[190:191]
	v_pk_add_f32 v[222:223], v[222:223], v[176:177]
	v_add_f32_e32 v172, v188, v189
	v_add_f32_e32 v174, v222, v223

.Lp6a2_954:
	s_lshr_b32 s66, s26, 14
	s_lshr_b32 s14, s86, 14
	s_cmp_lg_u32 s14, s66
	s_cselect_b64 s[0:1], -1, 0
.Lp6a2_956:
	s_bfe_u32 s36, s26, 0x4000a
	v_cvt_pk_f32_fp8_e32 v[184:185], v224
	v_cvt_pk_f32_fp8_e32 v[192:193], v228
	v_cvt_pk_f32_fp8_sdwa v[186:187], v224 src0_sel:WORD_1
	v_cvt_pk_f32_fp8_sdwa v[194:195], v228 src0_sel:WORD_1
	v_pk_mul_f32 v[188:189], v[184:185], v[144:145]
	v_pk_mul_f32 v[222:223], v[192:193], v[144:145]
	v_pk_mul_f32 v[190:191], v[186:187], v[146:147]
	v_pk_mul_f32 v[176:177], v[194:195], v[146:147]
	v_cvt_pk_f32_fp8_e32 v[184:185], v225
	v_cvt_pk_f32_fp8_e32 v[192:193], v229
	v_cvt_pk_f32_fp8_sdwa v[186:187], v225 src0_sel:WORD_1
	v_cvt_pk_f32_fp8_sdwa v[194:195], v229 src0_sel:WORD_1
	v_pk_fma_f32 v[188:189], v[184:185], v[148:149], v[188:189]
	v_pk_fma_f32 v[222:223], v[192:193], v[148:149], v[222:223]
	v_pk_fma_f32 v[190:191], v[186:187], v[150:151], v[190:191]
	v_pk_fma_f32 v[176:177], v[194:195], v[150:151], v[176:177]
	v_cvt_pk_f32_fp8_e32 v[184:185], v226
	v_cvt_pk_f32_fp8_e32 v[192:193], v230
	v_cvt_pk_f32_fp8_sdwa v[186:187], v226 src0_sel:WORD_1
	v_cvt_pk_f32_fp8_sdwa v[194:195], v230 src0_sel:WORD_1
	v_pk_fma_f32 v[188:189], v[184:185], v[152:153], v[188:189]
	v_pk_fma_f32 v[222:223], v[192:193], v[152:153], v[222:223]
	v_pk_fma_f32 v[190:191], v[186:187], v[154:155], v[190:191]
	v_pk_fma_f32 v[176:177], v[194:195], v[154:155], v[176:177]
	v_cvt_pk_f32_fp8_e32 v[184:185], v227
	v_cvt_pk_f32_fp8_e32 v[192:193], v231
	v_cvt_pk_f32_fp8_sdwa v[186:187], v227 src0_sel:WORD_1
	v_cvt_pk_f32_fp8_sdwa v[194:195], v231 src0_sel:WORD_1
	v_pk_fma_f32 v[188:189], v[184:185], v[156:157], v[188:189]
	v_pk_fma_f32 v[222:223], v[192:193], v[156:157], v[222:223]
	v_pk_fma_f32 v[190:191], v[186:187], v[158:159], v[190:191]
	v_pk_fma_f32 v[176:177], v[194:195], v[158:159], v[176:177]
	v_pk_add_f32 v[188:189], v[188:189], v[190:191]
	v_pk_add_f32 v[222:223], v[222:223], v[176:177]
	v_add_f32_e32 v160, v188, v189
	v_add_f32_e32 v162, v222, v223
	s_cmp_le_u32 s36, 2
	s_cbranch_scc1 .Lp6a2_dotdone
	v_cvt_pk_f32_fp8_e32 v[184:185], v232
	v_cvt_pk_f32_fp8_e32 v[192:193], v236
	v_cvt_pk_f32_fp8_sdwa v[186:187], v232 src0_sel:WORD_1
	v_cvt_pk_f32_fp8_sdwa v[194:195], v236 src0_sel:WORD_1
	v_pk_mul_f32 v[188:189], v[184:185], v[144:145]
	v_pk_mul_f32 v[222:223], v[192:193], v[144:145]
	v_pk_mul_f32 v[190:191], v[186:187], v[146:147]
	v_pk_mul_f32 v[176:177], v[194:195], v[146:147]
	v_cvt_pk_f32_fp8_e32 v[184:185], v233
	v_cvt_pk_f32_fp8_e32 v[192:193], v237
	v_cvt_pk_f32_fp8_sdwa v[186:187], v233 src0_sel:WORD_1
	v_cvt_pk_f32_fp8_sdwa v[194:195], v237 src0_sel:WORD_1
	v_pk_fma_f32 v[188:189], v[184:185], v[148:149], v[188:189]
	v_pk_fma_f32 v[222:223], v[192:193], v[148:149], v[222:223]
	v_pk_fma_f32 v[190:191], v[186:187], v[150:151], v[190:191]
	v_pk_fma_f32 v[176:177], v[194:195], v[150:151], v[176:177]
	v_cvt_pk_f32_fp8_e32 v[184:185], v234
	v_cvt_pk_f32_fp8_e32 v[192:193], v238
	v_cvt_pk_f32_fp8_sdwa v[186:187], v234 src0_sel:WORD_1
	v_cvt_pk_f32_fp8_sdwa v[194:195], v238 src0_sel:WORD_1
	v_pk_fma_f32 v[188:189], v[184:185], v[152:153], v[188:189]
	v_pk_fma_f32 v[222:223], v[192:193], v[152:153], v[222:223]
	v_pk_fma_f32 v[190:191], v[186:187], v[154:155], v[190:191]
	v_pk_fma_f32 v[176:177], v[194:195], v[154:155], v[176:177]
	v_cvt_pk_f32_fp8_e32 v[184:185], v235
	v_cvt_pk_f32_fp8_e32 v[192:193], v239
	v_cvt_pk_f32_fp8_sdwa v[186:187], v235 src0_sel:WORD_1
	v_cvt_pk_f32_fp8_sdwa v[194:195], v239 src0_sel:WORD_1
	v_pk_fma_f32 v[188:189], v[184:185], v[156:157], v[188:189]
	v_pk_fma_f32 v[222:223], v[192:193], v[156:157], v[222:223]
	v_pk_fma_f32 v[190:191], v[186:187], v[158:159], v[190:191]
	v_pk_fma_f32 v[176:177], v[194:195], v[158:159], v[176:177]
	v_pk_add_f32 v[188:189], v[188:189], v[190:191]
	v_pk_add_f32 v[222:223], v[222:223], v[176:177]
	v_add_f32_e32 v164, v188, v189
	v_add_f32_e32 v166, v222, v223
	s_cmp_le_u32 s36, 4
	s_cbranch_scc1 .Lp6a2_dotdone
	v_cvt_pk_f32_fp8_e32 v[184:185], v240
	v_cvt_pk_f32_fp8_e32 v[192:193], v244
	v_cvt_pk_f32_fp8_sdwa v[186:187], v240 src0_sel:WORD_1
	v_cvt_pk_f32_fp8_sdwa v[194:195], v244 src0_sel:WORD_1
	v_pk_mul_f32 v[188:189], v[184:185], v[144:145]
	v_pk_mul_f32 v[222:223], v[192:193], v[144:145]
	v_pk_mul_f32 v[190:191], v[186:187], v[146:147]
	v_pk_mul_f32 v[176:177], v[194:195], v[146:147]
	v_cvt_pk_f32_fp8_e32 v[184:185], v241
	v_cvt_pk_f32_fp8_e32 v[192:193], v245
	v_cvt_pk_f32_fp8_sdwa v[186:187], v241 src0_sel:WORD_1
	v_cvt_pk_f32_fp8_sdwa v[194:195], v245 src0_sel:WORD_1
	v_pk_fma_f32 v[188:189], v[184:185], v[148:149], v[188:189]
	v_pk_fma_f32 v[222:223], v[192:193], v[148:149], v[222:223]
	v_pk_fma_f32 v[190:191], v[186:187], v[150:151], v[190:191]
	v_pk_fma_f32 v[176:177], v[194:195], v[150:151], v[176:177]
	v_cvt_pk_f32_fp8_e32 v[184:185], v242
	v_cvt_pk_f32_fp8_e32 v[192:193], v246
	v_cvt_pk_f32_fp8_sdwa v[186:187], v242 src0_sel:WORD_1
	v_cvt_pk_f32_fp8_sdwa v[194:195], v246 src0_sel:WORD_1
	v_pk_fma_f32 v[188:189], v[184:185], v[152:153], v[188:189]
	v_pk_fma_f32 v[222:223], v[192:193], v[152:153], v[222:223]
	v_pk_fma_f32 v[190:191], v[186:187], v[154:155], v[190:191]
	v_pk_fma_f32 v[176:177], v[194:195], v[154:155], v[176:177]
	v_cvt_pk_f32_fp8_e32 v[184:185], v243
	v_cvt_pk_f32_fp8_e32 v[192:193], v247
	v_cvt_pk_f32_fp8_sdwa v[186:187], v243 src0_sel:WORD_1
	v_cvt_pk_f32_fp8_sdwa v[194:195], v247 src0_sel:WORD_1
	v_pk_fma_f32 v[188:189], v[184:185], v[156:157], v[188:189]
	v_pk_fma_f32 v[222:223], v[192:193], v[156:157], v[222:223]
	v_pk_fma_f32 v[190:191], v[186:187], v[158:159], v[190:191]
	v_pk_fma_f32 v[176:177], v[194:195], v[158:159], v[176:177]
	v_pk_add_f32 v[188:189], v[188:189], v[190:191]
	v_pk_add_f32 v[222:223], v[222:223], v[176:177]
	v_add_f32_e32 v168, v188, v189
	v_add_f32_e32 v170, v222, v223
	s_cmp_le_u32 s36, 6
	s_cbranch_scc1 .Lp6a2_dotdone
	v_cvt_pk_f32_fp8_e32 v[184:185], v248
	v_cvt_pk_f32_fp8_e32 v[192:193], v216
	v_cvt_pk_f32_fp8_sdwa v[186:187], v248 src0_sel:WORD_1
	v_cvt_pk_f32_fp8_sdwa v[194:195], v216 src0_sel:WORD_1
	v_pk_mul_f32 v[188:189], v[184:185], v[144:145]
	v_pk_mul_f32 v[222:223], v[192:193], v[144:145]
	v_pk_mul_f32 v[190:191], v[186:187], v[146:147]
	v_pk_mul_f32 v[176:177], v[194:195], v[146:147]
	v_cvt_pk_f32_fp8_e32 v[184:185], v249
	v_cvt_pk_f32_fp8_e32 v[192:193], v217
	v_cvt_pk_f32_fp8_sdwa v[186:187], v249 src0_sel:WORD_1
	v_cvt_pk_f32_fp8_sdwa v[194:195], v217 src0_sel:WORD_1
	v_pk_fma_f32 v[188:189], v[184:185], v[148:149], v[188:189]
	v_pk_fma_f32 v[222:223], v[192:193], v[148:149], v[222:223]
	v_pk_fma_f32 v[190:191], v[186:187], v[150:151], v[190:191]
	v_pk_fma_f32 v[176:177], v[194:195], v[150:151], v[176:177]
	v_cvt_pk_f32_fp8_e32 v[184:185], v250
	v_cvt_pk_f32_fp8_e32 v[192:193], v218
	v_cvt_pk_f32_fp8_sdwa v[186:187], v250 src0_sel:WORD_1
	v_cvt_pk_f32_fp8_sdwa v[194:195], v218 src0_sel:WORD_1
	v_pk_fma_f32 v[188:189], v[184:185], v[152:153], v[188:189]
	v_pk_fma_f32 v[222:223], v[192:193], v[152:153], v[222:223]
	v_pk_fma_f32 v[190:191], v[186:187], v[154:155], v[190:191]
	v_pk_fma_f32 v[176:177], v[194:195], v[154:155], v[176:177]
	v_cvt_pk_f32_fp8_e32 v[184:185], v251
	v_cvt_pk_f32_fp8_e32 v[192:193], v219
	v_cvt_pk_f32_fp8_sdwa v[186:187], v251 src0_sel:WORD_1
	v_cvt_pk_f32_fp8_sdwa v[194:195], v219 src0_sel:WORD_1
	v_pk_fma_f32 v[188:189], v[184:185], v[156:157], v[188:189]
	v_pk_fma_f32 v[222:223], v[192:193], v[156:157], v[222:223]
	v_pk_fma_f32 v[190:191], v[186:187], v[158:159], v[190:191]
	v_pk_fma_f32 v[176:177], v[194:195], v[158:159], v[176:177]
	v_pk_add_f32 v[188:189], v[188:189], v[190:191]
	v_pk_add_f32 v[222:223], v[222:223], v[176:177]
	v_add_f32_e32 v172, v188, v189
	v_add_f32_e32 v174, v222, v223
